# MOE1 K-loop: next unit's row-id mailbox requests read the expert/tile tables from LDS once instead of four times
# speedup vs baseline: 1.0073x; 1.0038x over previous
.Lpm_1248:
	s_cmp_eq_u32 s1, 4
	s_cselect_b64 s[42:43], -1, 0
	s_andn2_b64 vcc, exec, s[40:41]
	s_cbranch_vccnz .Lpm_1247
	s_cmp_lg_u32 s1, 2
	s_cbranch_scc1 .Lpm_1251
	v_mov_b32_e32 v4, s0
	ds_read_b32 v2, v4 offset:512
	s_mov_b32 m0, s71
	s_waitcnt lgkmcnt(0)
	v_readfirstlane_b32 s46, v2
	s_lshl_b32 s47, s46, 2
	s_add_i32 s47, s31, s47
	v_mov_b32_e32 v2, s47
	ds_read_b32 v3, v2 offset:32
	ds_read_b32 v2, v2 offset:192
	s_waitcnt lgkmcnt(0)
	v_readfirstlane_b32 s47, v3
	s_sub_i32 s49, s76, s47
	v_readfirstlane_b32 s48, v2
	s_add_i32 s48, s48, -1
	s_mul_hi_i32 s47, s46, 0x48000
	s_mul_i32 s46, s46, 0x48000
	s_add_u32 s46, s56, s46
	s_addc_u32 s47, s57, s47
	v_lshl_add_u32 v2, s49, 8, v177
	v_min_i32_e32 v2, s48, v2
	v_ashrrev_i32_e32 v3, 31, v2
	v_lshl_add_u64 v[2:3], v[2:3], 2, s[46:47]
	global_load_lds_dword v[2:3], off
	v_lshl_add_u32 v2, s49, 8, v178
	v_min_i32_e32 v2, s48, v2
	v_ashrrev_i32_e32 v3, 31, v2
	v_lshl_add_u64 v[2:3], v[2:3], 2, s[46:47]
	s_add_i32 m0, s71, 0x100
	s_nop 0
	global_load_lds_dword v[2:3], off
	v_lshl_add_u32 v2, s49, 8, v179
	v_min_i32_e32 v2, s48, v2
	v_ashrrev_i32_e32 v3, 31, v2
	v_lshl_add_u64 v[2:3], v[2:3], 2, s[46:47]
	s_add_i32 m0, s71, 0x200
	s_nop 0
	global_load_lds_dword v[2:3], off
	v_lshl_add_u32 v2, s49, 8, v180
	v_min_i32_e32 v2, s48, v2
	v_ashrrev_i32_e32 v3, 31, v2
	v_lshl_add_u64 v[2:3], v[2:3], 2, s[46:47]
	s_add_i32 m0, s71, 0x300
	s_nop 0
	global_load_lds_dword v[2:3], off
